# speedup vs baseline: 1.0142x; 1.0142x over previous
_Z5k_aggPKDF16_PKhPKiS4_PKDv8_DF16_PKfPDF16_Pf:
	s_load_dwordx8 s[4:11], s[0:1], 0x8
	s_load_dwordx4 s[12:15], s[0:1], 0x28
	s_load_dwordx2 s[16:17], s[0:1], 0x38
	v_lshlrev_b32_e32 v2, 4, v0
	s_lshl_b32 s0, s2, 2
	s_lshl_b32 s1, s2, 3
	s_andn2_b32 s0, s0, 63
	s_and_b32 s1, s1, 56
	s_or_b32 s0, s0, s1
	s_lshr_b32 s1, s2, 1
	s_and_b32 s1, s1, 4
	s_or_b32 s0, s0, s1
	v_lshlrev_b32_e32 v1, 2, v0
	v_lshrrev_b32_e32 v52, 6, v0
	v_or_b32_e32 v3, s0, v52
	v_mov_b32_e32 v98, v2
	s_waitcnt lgkmcnt(0)
	v_readfirstlane_b32 s19, v52
	s_nop 3
	s_lshl_b32 s19, s19, 10
	s_mov_b32 m0, s19
	s_nop 0
	global_load_lds_dwordx4 v2, s[10:11]
	s_add_u32 m0, s19, 0x1000
	v_add_u32_e32 v96, 0x1000, v2
	global_load_lds_dwordx4 v96, s[10:11]
	s_add_u32 m0, s19, 0x2000
	v_add_u32_e32 v96, 0x2000, v2
	global_load_lds_dwordx4 v96, s[10:11]
	s_add_u32 m0, s19, 0x3000
	v_add_u32_e32 v96, 0x3000, v2
	global_load_lds_dwordx4 v96, s[10:11]
	s_add_u32 m0, s19, 0x4000
	v_add_u32_e32 v96, 0x4000, v2
	global_load_lds_dwordx4 v96, s[10:11]
	s_add_u32 m0, s19, 0x5000
	v_add_u32_e32 v96, 0x5000, v2
	global_load_lds_dwordx4 v96, s[10:11]
	s_add_u32 m0, s19, 0x6000
	v_add_u32_e32 v96, 0x6000, v2
	global_load_lds_dwordx4 v96, s[10:11]
	s_add_u32 m0, s19, 0x7000
	v_add_u32_e32 v96, 0x7000, v2
	global_load_lds_dwordx4 v96, s[10:11]
	v_mov_b32_e32 v97, 0
	ds_write2st64_b32 v1, v97, v97 offset0:128 offset1:132
	ds_write2st64_b32 v1, v97, v97 offset0:136 offset1:140
	s_movk_i32 s0, 0x186a
	v_cmp_gt_i32_e32 vcc, s0, v3
	s_and_saveexec_b64 s[0:1], vcc
	s_cbranch_execz .Lagg_invalid
	v_bfe_u32 v4, v0, 2, 4
	v_lshlrev_b32_e32 v53, 4, v3
	v_or_b32_e32 v10, v53, v4
	v_and_b32_e32 v54, 48, v2
	v_lshl_or_b32 v11, v10, 7, v54
	global_load_dwordx4 v[2:5], v11, s[4:5]
	global_load_dwordx4 v[6:9], v11, s[4:5] offset:64
	v_ashrrev_i32_e32 v11, 31, v10
	v_lshl_add_u64 v[10:11], v[10:11], 2, s[6:7]
	global_load_dwordx2 v[50:51], v[10:11], off
	s_waitcnt vmcnt(2)
	v_cvt_pk_f32_fp8_e32 v[10:11], v2
	v_cvt_pk_f32_fp8_sdwa v[12:13], v2 src0_sel:WORD_1
	v_cvt_pk_f32_fp8_e32 v[14:15], v3
	v_cvt_pk_f32_fp8_sdwa v[2:3], v3 src0_sel:WORD_1
	v_cvt_pk_f32_fp8_e32 v[16:17], v4
	v_cvt_pk_f32_fp8_sdwa v[18:19], v4 src0_sel:WORD_1
	v_cvt_pk_f32_fp8_e32 v[20:21], v5
	v_cvt_pk_f32_fp8_sdwa v[4:5], v5 src0_sel:WORD_1
	s_waitcnt vmcnt(1)
	v_cvt_pk_f32_fp8_e32 v[22:23], v6
	v_cvt_pk_f32_fp8_sdwa v[24:25], v6 src0_sel:WORD_1
	v_cvt_pk_f32_fp8_e32 v[26:27], v7
	v_cvt_pk_f32_fp8_sdwa v[6:7], v7 src0_sel:WORD_1
	v_cvt_pk_f32_fp8_e32 v[28:29], v8
	v_cvt_pk_f32_fp8_sdwa v[30:31], v8 src0_sel:WORD_1
	v_cvt_pk_f32_fp8_e32 v[32:33], v9
	v_cvt_pk_f32_fp8_sdwa v[8:9], v9 src0_sel:WORD_1
	v_add_f32_e32 v88, 0, v10
	v_add_f32_e32 v89, 0, v11
	v_add_f32_e32 v90, 0, v12
	v_add_f32_e32 v91, 0, v13
	v_add_f32_e32 v92, 0, v14
	v_add_f32_e32 v93, 0, v15
	v_add_f32_e32 v94, 0, v2
	v_add_f32_e32 v95, 0, v3
	v_add_f32_e32 v76, 0, v16
	v_add_f32_e32 v77, 0, v17
	v_add_f32_e32 v80, 0, v18
	v_add_f32_e32 v81, 0, v19
	v_add_f32_e32 v84, 0, v20
	v_add_f32_e32 v85, 0, v21
	v_add_f32_e32 v86, 0, v4
	v_add_f32_e32 v87, 0, v5
	v_add_f32_e32 v72, 0, v22
	v_add_f32_e32 v73, 0, v23
	v_add_f32_e32 v74, 0, v24
	v_add_f32_e32 v75, 0, v25
	v_add_f32_e32 v78, 0, v26
	v_add_f32_e32 v79, 0, v27
	v_add_f32_e32 v82, 0, v6
	v_add_f32_e32 v83, 0, v7
	v_add_f32_e32 v64, 0, v28
	v_add_f32_e32 v65, 0, v29
	v_add_f32_e32 v66, 0, v30
	v_add_f32_e32 v67, 0, v31
	v_add_f32_e32 v68, 0, v32
	v_add_f32_e32 v69, 0, v33
	v_add_f32_e32 v70, 0, v8
	v_add_f32_e32 v71, 0, v9
	s_waitcnt vmcnt(0)
	s_mov_b64 s[6:7], exec
	v_mov_b32_e32 v63, 0xc35000
	v_add_u32_e32 v106, 0, v50
	v_lshlrev_b32_e32 v106, 2, v106
	global_load_dwordx3 v[56:58], v106, s[8:9]
	v_add_u32_e32 v106, 3, v50
	v_lshlrev_b32_e32 v106, 2, v106
	global_load_dwordx3 v[60:62], v106, s[8:9]
	s_waitcnt vmcnt(0)
	v_add_u32_e32 v104, 0, v50
	v_cmp_lt_i32_e32 vcc, v104, v51
	v_lshlrev_b32_e32 v105, 7, v56
	s_nop 0
	v_cndmask_b32_e32 v105, v63, v105, vcc
	v_or_b32_e32 v105, v54, v105
	global_load_dwordx4 v[2:5], v105, s[4:5]
	global_load_dwordx4 v[6:9], v105, s[4:5] offset:64
	v_add_u32_e32 v104, 1, v50
	v_cmp_lt_i32_e32 vcc, v104, v51
	v_lshlrev_b32_e32 v105, 7, v57
	s_nop 0
	v_cndmask_b32_e32 v105, v63, v105, vcc
	v_or_b32_e32 v105, v54, v105
	global_load_dwordx4 v[10:13], v105, s[4:5]
	global_load_dwordx4 v[14:17], v105, s[4:5] offset:64
	v_add_u32_e32 v104, 2, v50
	v_cmp_lt_i32_e32 vcc, v104, v51
	v_lshlrev_b32_e32 v105, 7, v58
	s_nop 0
	v_cndmask_b32_e32 v105, v63, v105, vcc
	v_or_b32_e32 v105, v54, v105
	global_load_dwordx4 v[18:21], v105, s[4:5]
	global_load_dwordx4 v[22:25], v105, s[4:5] offset:64
	v_add_u32_e32 v106, 6, v50
	v_lshlrev_b32_e32 v106, 2, v106
	global_load_dwordx3 v[56:58], v106, s[8:9]
	v_add_u32_e32 v104, 3, v50
	v_cmp_lt_i32_e32 vcc, v104, v51
	v_lshlrev_b32_e32 v105, 7, v60
	s_nop 0
	v_cndmask_b32_e32 v105, v63, v105, vcc
	v_or_b32_e32 v105, v54, v105
	global_load_dwordx4 v[26:29], v105, s[4:5]
	global_load_dwordx4 v[30:33], v105, s[4:5] offset:64
	v_add_u32_e32 v104, 4, v50
	v_cmp_lt_i32_e32 vcc, v104, v51
	v_lshlrev_b32_e32 v105, 7, v61
	s_nop 0
	v_cndmask_b32_e32 v105, v63, v105, vcc
	v_or_b32_e32 v105, v54, v105
	global_load_dwordx4 v[34:37], v105, s[4:5]
	global_load_dwordx4 v[38:41], v105, s[4:5] offset:64
	v_add_u32_e32 v104, 5, v50
	v_cmp_lt_i32_e32 vcc, v104, v51
	v_lshlrev_b32_e32 v105, 7, v62
	s_nop 0
	v_cndmask_b32_e32 v105, v63, v105, vcc
	v_or_b32_e32 v105, v54, v105
	global_load_dwordx4 v[42:45], v105, s[4:5]
	global_load_dwordx4 v[46:49], v105, s[4:5] offset:64
	v_add_u32_e32 v106, 9, v50
	v_lshlrev_b32_e32 v106, 2, v106
	global_load_dwordx3 v[60:62], v106, s[8:9]

.LBB5_2:
	s_or_b64 exec, exec, s[4:5]
	s_movk_i32 s4, 0xc2a
	v_add_u32_e32 v97, 0xc40, v1
	v_cmp_gt_i32_e64 s[4:5], s4, v1
	s_load_dwordx2 s[6:7], s[0:1], 0x48
	s_load_dwordx4 s[8:11], s[0:1], 0x28
	s_movk_i32 s12, 0x80
	v_and_b32_e32 v71, 63, v0
	v_cmp_gt_u32_e32 vcc, s12, v0
	v_lshlrev_b32_e32 v26, 2, v0
	s_and_saveexec_b64 s[12:13], vcc
	s_xor_b64 s[16:17], exec, s[12:13]
	s_cbranch_execz .LBB5_6
	s_load_dwordx4 s[12:15], s[0:1], 0x8
	s_nop 0
	s_load_dwordx2 s[0:1], s[0:1], 0x18
	v_mov_b32_e32 v27, 0
	s_movk_i32 s18, 0x1000
	s_waitcnt lgkmcnt(0)
	v_lshl_add_u64 v[72:73], s[12:13], 0, v[26:27]
	global_load_dword v27, v26, s[12:13]
	global_load_dword v29, v26, s[12:13] offset:512
	global_load_dword v76, v26, s[12:13] offset:1024
	global_load_dword v78, v26, s[12:13] offset:1536
	global_load_dword v80, v26, s[12:13] offset:2048
	global_load_dword v84, v26, s[12:13] offset:2560
	global_load_dword v86, v26, s[12:13] offset:3072
	global_load_dword v88, v26, s[12:13] offset:3584
	v_add_co_u32_e32 v72, vcc, s18, v72
	s_mov_b32 s12, 0x800000
	s_nop 0
	v_addc_co_u32_e32 v73, vcc, 0, v73, vcc
	global_load_dword v90, v[72:73], off
	global_load_dword v91, v[72:73], off offset:512
	global_load_dword v92, v[72:73], off offset:1024
	global_load_dword v93, v[72:73], off offset:1536
	global_load_dword v95, v[72:73], off offset:2048
	global_load_dword v96, v[72:73], off offset:2560
	global_load_dword v102, v[72:73], off offset:3072
	global_load_dword v104, v[72:73], off offset:3584
	global_load_dword v106, v26, s[14:15]
	global_load_dword v107, v26, s[0:1]
	s_mov_b32 s0, 0x88e368f1
	s_mov_b32 s1, 0x3ee4f8b5
	s_waitcnt vmcnt(17)
	v_cvt_f64_f32_e32 v[72:73], v27
	v_add_f64 v[72:73], v[72:73], 0
	s_waitcnt vmcnt(15)
	v_cvt_f64_f32_e32 v[76:77], v76
	v_cvt_f64_f32_e32 v[74:75], v29
	s_waitcnt vmcnt(13)
	v_cvt_f64_f32_e32 v[80:81], v80
	v_add_f64 v[72:73], v[72:73], v[76:77]
	v_cvt_f64_f32_e32 v[78:79], v78
	s_waitcnt vmcnt(11)
	v_cvt_f64_f32_e32 v[86:87], v86
	v_add_f64 v[74:75], v[74:75], 0
	v_add_f64 v[72:73], v[72:73], v[80:81]
	v_cvt_f64_f32_e32 v[84:85], v84
	v_add_f64 v[74:75], v[74:75], v[78:79]
	s_waitcnt vmcnt(9)
	v_cvt_f64_f32_e32 v[76:77], v90
	v_add_f64 v[72:73], v[72:73], v[86:87]
	v_cvt_f64_f32_e32 v[88:89], v88
	s_waitcnt vmcnt(8)
	v_cvt_f64_f32_e32 v[78:79], v91
	s_waitcnt vmcnt(7)
	v_cvt_f64_f32_e32 v[90:91], v92
	v_add_f64 v[74:75], v[74:75], v[84:85]
	v_add_f64 v[72:73], v[72:73], v[76:77]
	s_waitcnt vmcnt(5)
	v_cvt_f64_f32_e32 v[98:99], v95
	v_add_f64 v[74:75], v[74:75], v[88:89]
	v_add_f64 v[72:73], v[72:73], v[90:91]
	v_cvt_f64_f32_e32 v[92:93], v93
	s_waitcnt vmcnt(3)
	v_cvt_f64_f32_e32 v[102:103], v102
	v_add_f64 v[74:75], v[74:75], v[78:79]
	v_add_f64 v[72:73], v[72:73], v[98:99]
	v_cvt_f64_f32_e32 v[100:101], v96
	v_add_f64 v[74:75], v[74:75], v[92:93]
	v_add_f64 v[72:73], v[72:73], v[102:103]
	s_waitcnt vmcnt(2)
	v_cvt_f64_f32_e32 v[104:105], v104
	v_add_f64 v[74:75], v[74:75], v[100:101]
	v_mul_f64 v[72:73], v[72:73], s[0:1]
	v_add_f64 v[74:75], v[74:75], v[104:105]
	v_mul_f64 v[76:77], v[72:73], v[72:73]
	v_fma_f64 v[74:75], v[74:75], s[0:1], -v[76:77]
	v_max_f64 v[74:75], v[74:75], 0
	v_cvt_f32_f64_e32 v27, v[74:75]
	v_add_f32_e32 v27, 0x3727c5ac, v27
	v_mul_f32_e32 v29, 0x4b800000, v27
	v_cmp_gt_f32_e32 vcc, s12, v27
	s_nop 1
	v_cndmask_b32_e32 v27, v27, v29, vcc
	v_rsq_f32_e32 v27, v27
	s_nop 0
	v_mul_f32_e32 v29, 0x45800000, v27
	v_cndmask_b32_e32 v27, v27, v29, vcc
	s_waitcnt vmcnt(1)
	v_mul_f32_e32 v27, v106, v27
	v_cvt_f32_f64_e32 v29, v[72:73]
	s_waitcnt vmcnt(0)
	v_fma_f32 v29, -v27, v29, v107
	ds_write2st64_b32 v26, v27, v29 offset1:2
.LBB5_6:
	s_or_b64 exec, exec, s[16:17]
	v_mov_b32_e32 v29, 0
	v_and_b32_e32 v0, 15, v0
	v_lshrrev_b32_e32 v27, 4, v71
	s_waitcnt lgkmcnt(0)
	v_lshl_add_u64 v[84:85], s[8:9], 0, v[28:29]
	v_lshlrev_b32_e32 v28, 4, v71
	v_cmp_gt_u32_e32 vcc, 10, v0
	v_lshlrev_b32_e32 v0, 4, v0
	v_and_or_b32 v26, v26, 60, v27
	v_lshl_add_u64 v[88:89], s[10:11], 0, v[28:29]
	v_lshlrev_b32_e32 v28, 1, v0
	v_and_b32_e32 v0, 12, v94
	v_lshlrev_b32_e32 v70, 3, v70
	v_lshlrev_b32_e32 v95, 2, v26
	v_lshl_add_u64 v[26:27], s[6:7], 0, v[28:29]
	v_lshlrev_b32_e32 v28, 1, v0
	v_lshl_add_u64 v[86:87], v[26:27], 0, v[28:29]
	v_lshlrev_b32_e32 v96, 2, v70
	s_barrier
	s_and_saveexec_b64 s[0:1], s[2:3]
	s_cbranch_execz .LBB5_9
	v_lshlrev_b32_e32 v0, 4, v1
	ds_read_b128 v[70:73], v96
	ds_read_b128 v[74:77], v96 offset:512
	v_or_b32_e32 v90, v0, v94
	v_ashrrev_i32_e32 v91, 31, v90
	v_lshlrev_b64 v[26:27], 8, v[90:91]
	v_lshl_add_u64 v[92:93], v[82:83], 0, v[26:27]
	s_waitcnt vmcnt(0)
	s_and_saveexec_b64 s[20:21], s[4:5]
	s_cbranch_execz .LBB5_4
	v_lshl_or_b32 v2, v97, 4, v94
	v_ashrrev_i32_e32 v3, 31, v2
	v_lshlrev_b64 v[2:3], 8, v[2:3]
	v_lshl_add_u64 v[4:5], v[4:5], 0, v[2:3]
	v_lshl_add_u64 v[6:7], v[82:83], 0, v[2:3]
	global_load_dwordx4 v[38:41], v[4:5], off
	global_load_dwordx4 v[18:21], v[4:5], off offset:64
	global_load_dwordx4 v[42:45], v[6:7], off
	global_load_dwordx4 v[22:25], v[6:7], off offset:64
	global_load_dwordx4 v[10:13], v[4:5], off offset:128
	s_nop 0
	global_load_dwordx4 v[2:5], v[4:5], off offset:192
	s_nop 0
	global_load_dwordx4 v[14:17], v[6:7], off offset:128
	s_nop 0
	global_load_dwordx4 v[6:9], v[6:7], off offset:192
.LBB5_4:
	s_or_b64 exec, exec, s[20:21]
	v_cvt_f32_f16_sdwa v27, v66 dst_sel:DWORD dst_unused:UNUSED_PAD src0_sel:WORD_1
	v_cvt_f32_f16_e32 v26, v66
	s_waitcnt lgkmcnt(0)
	v_fma_mix_f32 v1, v70, v62, v74 op_sel_hi:[0,1,0]
	v_max_f32_e32 v70, 0, v1
	v_fma_mix_f32 v1, v71, v62, v75 op_sel:[0,1,0] op_sel_hi:[0,1,0]
	v_max_f32_e32 v71, 0, v1
	ds_read_b128 v[78:81], v96 offset:16
	ds_read_b128 v[98:101], v96 offset:528
	v_pk_add_f32 v[26:27], v[70:71], v[26:27]
	v_cvt_f32_f16_sdwa v71, v67 dst_sel:DWORD dst_unused:UNUSED_PAD src0_sel:WORD_1
	v_cvt_f32_f16_e32 v70, v67
	v_fma_mix_f32 v1, v72, v63, v76 op_sel_hi:[0,1,0]
	v_max_f32_e32 v62, 0, v1
	v_fma_mix_f32 v1, v73, v63, v77 op_sel:[0,1,0] op_sel_hi:[0,1,0]
	v_max_f32_e32 v63, 0, v1
	v_pk_add_f32 v[70:71], v[62:63], v[70:71]
	v_cvt_f32_f16_sdwa v63, v68 dst_sel:DWORD dst_unused:UNUSED_PAD src0_sel:WORD_1
	v_cvt_f32_f16_e32 v62, v68
	s_waitcnt lgkmcnt(0)
	v_fma_mix_f32 v1, v78, v64, v98 op_sel_hi:[0,1,0]
	v_max_f32_e32 v72, 0, v1
	v_fma_mix_f32 v1, v79, v64, v99 op_sel:[0,1,0] op_sel_hi:[0,1,0]
	v_cvt_f32_f16_sdwa v75, v69 dst_sel:DWORD dst_unused:UNUSED_PAD src0_sel:WORD_1
	v_cvt_f32_f16_e32 v74, v69
	v_max_f32_e32 v73, 0, v1
	v_fma_mix_f32 v1, v80, v65, v100 op_sel_hi:[0,1,0]
	v_pk_add_f32 v[72:73], v[72:73], v[62:63]
	v_max_f32_e32 v64, 0, v1
	v_fma_mix_f32 v1, v81, v65, v101 op_sel:[0,1,0] op_sel_hi:[0,1,0]
	v_mov_b32_e32 v62, v29
	v_max_f32_e32 v65, 0, v1
	v_cvt_pk_fp8_f32 v62, v26, v27
	v_cvt_pk_f16_f32 v66, v26, v27
	v_pk_add_f32 v[26:27], v[64:65], v[74:75]
	v_cvt_pk_f16_f32 v67, v70, v71
	v_cvt_pk_f16_f32 v68, v72, v73
	v_cvt_pk_f16_f32 v69, v26, v27
	v_mov_b32_e32 v63, v29
	global_store_dwordx4 v[92:93], v[66:69], off
	v_cvt_pk_fp8_f32 v63, v72, v73
	v_cvt_pk_fp8_f32 v62, v70, v71 op_sel:[0,0,1]
	ds_read_b128 v[70:73], v96 offset:128
	ds_read_b128 v[74:77], v96 offset:640
	ds_read_b128 v[78:81], v96 offset:144
	ds_read_b128 v[98:101], v96 offset:656
	v_cvt_pk_fp8_f32 v63, v26, v27 op_sel:[0,0,1]
	s_nop 0
	v_cvt_f32_f16_sdwa v27, v58 dst_sel:DWORD dst_unused:UNUSED_PAD src0_sel:WORD_1
	v_cvt_f32_f16_e32 v26, v58
	s_waitcnt lgkmcnt(2)
	v_fma_mix_f32 v1, v70, v54, v74 op_sel_hi:[0,1,0]
	v_max_f32_e32 v64, 0, v1
	v_fma_mix_f32 v1, v71, v54, v75 op_sel:[0,1,0] op_sel_hi:[0,1,0]
	v_max_f32_e32 v65, 0, v1
	v_pk_add_f32 v[26:27], v[64:65], v[26:27]
	v_cvt_f32_f16_sdwa v65, v59 dst_sel:DWORD dst_unused:UNUSED_PAD src0_sel:WORD_1
	v_cvt_f32_f16_e32 v64, v59
	v_fma_mix_f32 v1, v72, v55, v76 op_sel_hi:[0,1,0]
	v_max_f32_e32 v58, 0, v1
	v_fma_mix_f32 v1, v73, v55, v77 op_sel:[0,1,0] op_sel_hi:[0,1,0]
	v_max_f32_e32 v59, 0, v1
	v_pk_add_f32 v[58:59], v[58:59], v[64:65]
	v_cvt_f32_f16_sdwa v65, v60 dst_sel:DWORD dst_unused:UNUSED_PAD src0_sel:WORD_1
	v_cvt_f32_f16_e32 v64, v60
	s_waitcnt lgkmcnt(0)
	v_fma_mix_f32 v1, v78, v56, v98 op_sel_hi:[0,1,0]
	v_max_f32_e32 v70, 0, v1
	v_fma_mix_f32 v1, v79, v56, v99 op_sel:[0,1,0] op_sel_hi:[0,1,0]
	v_cvt_f32_f16_sdwa v75, v61 dst_sel:DWORD dst_unused:UNUSED_PAD src0_sel:WORD_1
	v_cvt_f32_f16_e32 v74, v61
	v_max_f32_e32 v71, 0, v1
	v_fma_mix_f32 v1, v80, v57, v100 op_sel_hi:[0,1,0]
	v_pk_add_f32 v[70:71], v[70:71], v[64:65]
	v_max_f32_e32 v72, 0, v1
	v_fma_mix_f32 v1, v81, v57, v101 op_sel:[0,1,0] op_sel_hi:[0,1,0]
	v_mov_b32_e32 v64, v29
	v_max_f32_e32 v73, 0, v1
	v_cvt_pk_fp8_f32 v64, v26, v27
	v_cvt_pk_f16_f32 v54, v26, v27
	v_pk_add_f32 v[26:27], v[72:73], v[74:75]
	v_cvt_pk_f16_f32 v55, v58, v59
	v_cvt_pk_f16_f32 v56, v70, v71
	v_cvt_pk_f16_f32 v57, v26, v27
	v_mov_b32_e32 v65, v29
	global_store_dwordx4 v[92:93], v[54:57], off offset:64
	v_cvt_pk_fp8_f32 v65, v70, v71
	v_cvt_pk_fp8_f32 v64, v58, v59 op_sel:[0,0,1]
	ds_read_b128 v[58:61], v96 offset:256
	ds_read_b128 v[70:73], v96 offset:768
	ds_read_b128 v[74:77], v96 offset:272
	ds_read_b128 v[78:81], v96 offset:784
	global_load_dwordx4 v[98:101], v[88:89], off
	global_load_dwordx4 v[102:105], v[88:89], off offset:1024
	v_cvt_pk_fp8_f32 v65, v26, v27 op_sel:[0,0,1]
	s_nop 0
	v_cvt_f32_f16_sdwa v27, v50 dst_sel:DWORD dst_unused:UNUSED_PAD src0_sel:WORD_1
	v_cvt_f32_f16_e32 v26, v50
	s_waitcnt lgkmcnt(2)
	v_fma_mix_f32 v1, v58, v46, v70 op_sel_hi:[0,1,0]
	v_max_f32_e32 v58, 0, v1
	v_fma_mix_f32 v1, v59, v46, v71 op_sel:[0,1,0] op_sel_hi:[0,1,0]
	v_max_f32_e32 v59, 0, v1
	v_fma_mix_f32 v1, v60, v47, v72 op_sel_hi:[0,1,0]
	v_pk_add_f32 v[58:59], v[58:59], v[26:27]
	v_max_f32_e32 v26, 0, v1
	v_cvt_f32_f16_sdwa v107, v51 dst_sel:DWORD dst_unused:UNUSED_PAD src0_sel:WORD_1
	v_cvt_f32_f16_e32 v106, v51
	v_fma_mix_f32 v1, v61, v47, v73 op_sel:[0,1,0] op_sel_hi:[0,1,0]
	global_load_dwordx4 v[70:73], v[88:89], off offset:2048
	v_max_f32_e32 v27, 0, v1
	v_pk_add_f32 v[50:51], v[26:27], v[106:107]
	global_load_dwordx4 v[106:109], v[88:89], off offset:3072
	s_waitcnt lgkmcnt(0)
	v_fma_mix_f32 v1, v74, v48, v78 op_sel_hi:[0,1,0]
	v_cvt_f32_f16_sdwa v27, v52 dst_sel:DWORD dst_unused:UNUSED_PAD src0_sel:WORD_1
	v_cvt_f32_f16_e32 v26, v52
	v_max_f32_e32 v60, 0, v1
	v_fma_mix_f32 v1, v75, v48, v79 op_sel:[0,1,0] op_sel_hi:[0,1,0]
	v_max_f32_e32 v61, 0, v1
	v_fma_mix_f32 v1, v76, v49, v80 op_sel_hi:[0,1,0]
	v_max_f32_e32 v74, 0, v1
	v_fma_mix_f32 v1, v77, v49, v81 op_sel:[0,1,0] op_sel_hi:[0,1,0]
	v_cvt_f32_f16_sdwa v77, v53 dst_sel:DWORD dst_unused:UNUSED_PAD src0_sel:WORD_1
	v_cvt_f32_f16_e32 v76, v53
	v_pk_add_f32 v[60:61], v[60:61], v[26:27]
	v_mov_b32_e32 v26, v29
	v_mov_b32_e32 v27, v29
	v_max_f32_e32 v75, 0, v1
	v_cvt_pk_fp8_f32 v26, v58, v59
	v_cvt_pk_fp8_f32 v27, v60, v61
	v_pk_add_f32 v[52:53], v[74:75], v[76:77]
	v_cvt_pk_f16_f32 v46, v58, v59
	v_cvt_pk_f16_f32 v47, v50, v51
	v_cvt_pk_f16_f32 v48, v60, v61
	v_cvt_pk_f16_f32 v49, v52, v53
	global_store_dwordx4 v[92:93], v[46:49], off offset:128
	v_cvt_pk_fp8_f32 v26, v50, v51 op_sel:[0,0,1]
	v_cvt_pk_fp8_f32 v27, v52, v53 op_sel:[0,0,1]
	ds_read_b128 v[50:53], v96 offset:384
	ds_read_b128 v[58:61], v96 offset:896
	ds_read_b128 v[74:77], v96 offset:400
	ds_read_b128 v[78:81], v96 offset:912
	ds_bpermute_b32 v66, v95, v66
	ds_bpermute_b32 v67, v95, v67
	ds_bpermute_b32 v68, v95, v68
	s_waitcnt lgkmcnt(5)
	v_fma_mix_f32 v1, v50, v30, v58 op_sel_hi:[0,1,0]
	ds_bpermute_b32 v69, v95, v69
	v_max_f32_e32 v50, 0, v1
	v_fma_mix_f32 v1, v51, v30, v59 op_sel:[0,1,0] op_sel_hi:[0,1,0]
	s_nop 0
	v_cvt_f32_f16_sdwa v59, v35 dst_sel:DWORD dst_unused:UNUSED_PAD src0_sel:WORD_1
	v_cvt_f32_f16_e32 v58, v35
	v_max_f32_e32 v51, 0, v1
	v_fma_mix_f32 v1, v52, v31, v60 op_sel_hi:[0,1,0]
	v_cvt_f32_f16_sdwa v111, v34 dst_sel:DWORD dst_unused:UNUSED_PAD src0_sel:WORD_1
	v_cvt_f32_f16_e32 v110, v34
	v_max_f32_e32 v34, 0, v1
	v_fma_mix_f32 v1, v53, v31, v61 op_sel:[0,1,0] op_sel_hi:[0,1,0]
	v_cvt_f32_f16_sdwa v53, v36 dst_sel:DWORD dst_unused:UNUSED_PAD src0_sel:WORD_1
	v_cvt_f32_f16_e32 v52, v36
	v_max_f32_e32 v35, 0, v1
	s_waitcnt lgkmcnt(4)
	v_fma_mix_f32 v1, v74, v32, v78 op_sel_hi:[0,1,0]
	ds_bpermute_b32 v54, v95, v54
	ds_bpermute_b32 v55, v95, v55
	ds_bpermute_b32 v56, v95, v56
	ds_bpermute_b32 v57, v95, v57
	v_pk_add_f32 v[34:35], v[34:35], v[58:59]
	v_max_f32_e32 v58, 0, v1
	v_fma_mix_f32 v1, v75, v32, v79 op_sel:[0,1,0] op_sel_hi:[0,1,0]
	v_max_f32_e32 v59, 0, v1
	v_pk_add_f32 v[52:53], v[58:59], v[52:53]
	v_cvt_f32_f16_sdwa v59, v37 dst_sel:DWORD dst_unused:UNUSED_PAD src0_sel:WORD_1
	v_cvt_f32_f16_e32 v58, v37
	v_pk_add_f32 v[50:51], v[50:51], v[110:111]
	v_fma_mix_f32 v1, v76, v33, v80 op_sel_hi:[0,1,0]
	v_mov_b32_e32 v28, v29
	ds_bpermute_b32 v46, v95, v46
	ds_bpermute_b32 v47, v95, v47
	ds_bpermute_b32 v48, v95, v48
	ds_bpermute_b32 v49, v95, v49
	v_max_f32_e32 v36, 0, v1
	v_fma_mix_f32 v1, v77, v33, v81 op_sel:[0,1,0] op_sel_hi:[0,1,0]
	v_cvt_pk_fp8_f32 v28, v50, v51
	v_cvt_pk_f16_f32 v30, v50, v51
	v_cvt_pk_f16_f32 v32, v52, v53
	v_max_f32_e32 v37, 0, v1
	v_cvt_pk_fp8_f32 v29, v52, v53
	s_waitcnt vmcnt(4) lgkmcnt(8)
	v_mfma_f32_16x16x32_f16 v[50:53], v[66:69], v[98:101], 0
	v_add_f32_e64 v58, v36, v58
	v_add_f32_e64 v59, v37, v59
	v_cvt_pk_f16_f32 v31, v34, v35
	v_cvt_pk_f16_f32 v33, v58, v59
	v_cvt_pk_fp8_f32 v28, v34, v35 op_sel:[0,0,1]
	ds_bpermute_b32 v34, v95, v30
	ds_bpermute_b32 v35, v95, v31
	ds_bpermute_b32 v36, v95, v32
	ds_bpermute_b32 v37, v95, v33
	s_waitcnt vmcnt(3) lgkmcnt(8)
	v_mfma_f32_16x16x32_f16 v[50:53], v[54:57], v[102:105], v[50:53]
	global_store_dwordx4 v[92:93], v[30:33], off offset:192
	v_cvt_pk_fp8_f32 v29, v58, v59 op_sel:[0,0,1]
	v_lshlrev_b64 v[54:55], 7, v[90:91]
	s_waitcnt vmcnt(3) lgkmcnt(4)
	v_mfma_f32_16x16x32_f16 v[30:33], v[46:49], v[70:73], v[50:53]
	v_lshl_add_u64 v[46:47], v[84:85], 0, v[54:55]
	global_store_dwordx4 v[46:47], v[62:65], off
	global_store_dwordx4 v[46:47], v[26:29], off offset:64
	s_waitcnt vmcnt(4) lgkmcnt(0)
	s_nop 0
	v_mfma_f32_16x16x32_f16 v[26:29], v[34:37], v[106:109], v[30:33]
	s_and_b64 exec, exec, vcc
	s_cbranch_execz .LBB5_9
	v_mul_u32_u24_e32 v0, 10, v0
	v_ashrrev_i32_e32 v1, 31, v0
	v_lshl_add_u64 v[0:1], v[0:1], 1, v[86:87]
	global_load_dwordx2 v[30:31], v[0:1], off
	s_waitcnt vmcnt(0)
	v_cvt_f32_f16_e32 v32, v30
	v_cvt_f32_f16_sdwa v33, v30 dst_sel:DWORD dst_unused:UNUSED_PAD src0_sel:WORD_1
	v_cvt_f32_f16_e32 v30, v31
	v_cvt_f32_f16_sdwa v31, v31 dst_sel:DWORD dst_unused:UNUSED_PAD src0_sel:WORD_1
	v_pk_add_f32 v[26:27], v[26:27], v[32:33]
	s_nop 0
	v_cvt_pk_f16_f32 v26, v26, v27
	v_pk_add_f32 v[28:29], v[28:29], v[30:31]
	s_nop 0
	v_cvt_pk_f16_f32 v27, v28, v29
	global_store_dwordx2 v[0:1], v[26:27], off

	.amdhsa_kernel _Z8k_updateILi1EEvPKDF16_PKfS3_S3_PDF16_PhPKDv8_DF16_PKiPfSB_
		.amdhsa_group_segment_fixed_size 1024
		.amdhsa_private_segment_fixed_size 0
		.amdhsa_kernarg_size 80
		.amdhsa_user_sgpr_count 2
		.amdhsa_user_sgpr_dispatch_ptr 0
		.amdhsa_user_sgpr_queue_ptr 0
		.amdhsa_user_sgpr_kernarg_segment_ptr 1
		.amdhsa_user_sgpr_dispatch_id 0
		.amdhsa_user_sgpr_kernarg_preload_length 0
		.amdhsa_user_sgpr_kernarg_preload_offset 0
		.amdhsa_user_sgpr_private_segment_size 0
		.amdhsa_uses_dynamic_stack 0
		.amdhsa_enable_private_segment 0
		.amdhsa_system_sgpr_workgroup_id_x 1
		.amdhsa_system_sgpr_workgroup_id_y 0
		.amdhsa_system_sgpr_workgroup_id_z 0
		.amdhsa_system_sgpr_workgroup_info 0
		.amdhsa_system_vgpr_workitem_id 0
		.amdhsa_next_free_vgpr 112
		.amdhsa_next_free_sgpr 22
		.amdhsa_accum_offset 112
		.amdhsa_reserve_vcc 1
		.amdhsa_float_round_mode_32 0
		.amdhsa_float_round_mode_16_64 0
		.amdhsa_float_denorm_mode_32 3
		.amdhsa_float_denorm_mode_16_64 3
		.amdhsa_dx10_clamp 1
		.amdhsa_ieee_mode 1
		.amdhsa_fp16_overflow 0
		.amdhsa_tg_split 0
		.amdhsa_exception_fp_ieee_invalid_op 0
		.amdhsa_exception_fp_denorm_src 0
		.amdhsa_exception_fp_ieee_div_zero 0
		.amdhsa_exception_fp_ieee_overflow 0
		.amdhsa_exception_fp_ieee_underflow 0
		.amdhsa_exception_fp_ieee_inexact 0
		.amdhsa_exception_int_div_zero 0
	.end_amdhsa_kernel
